# speedup vs baseline: 1.0241x; 1.0241x over previous
.LBB0_19:
	s_and_b64 vcc, exec, s[6:7]
	s_cbranch_vccz .LBB0_56
	s_add_i32 s8, s2, 0xfffffee0
	v_subrev_co_u32_e64 v9, s[2:3], 14, v0
	v_subrev_co_u32_e32 v7, vcc, 28, v0
	s_load_dwordx4 s[12:15], s[0:1], 0x0
	s_load_dwordx2 s[6:7], s[0:1], 0x10
	v_cndmask_b32_e32 v1, 0, v9, vcc
	v_cndmask_b32_e64 v2, v1, v0, s[2:3]
	v_cmp_gt_u32_e64 s[2:3], -14, v7
	s_ashr_i32 s9, s8, 31
	v_mov_b32_e32 v5, 0
	v_cndmask_b32_e64 v1, 14, 0, s[2:3]
	v_add_u32_e32 v1, v1, v2
	v_mul_i32_i24_e32 v4, 3, v1
	s_lshl_b64 s[2:3], s[8:9], 11
	s_waitcnt lgkmcnt(0)
	v_lshl_add_u64 v[54:55], v[4:5], 2, s[4:5]
	v_lshrrev_b32_e32 v6, 4, v0
	s_movk_i32 s10, 0xe0
	s_add_u32 s4, s12, s2
	s_addc_u32 s5, s13, s3
	v_lshlrev_b32_e32 v3, 9, v6
	v_mov_b32_e32 v8, 0x1a00
	v_cmp_gt_u32_e64 s[2:3], s10, v0
	v_and_b32_e32 v1, 15, v0
	v_mov_b32_e32 v11, v5
	v_cndmask_b32_e64 v3, v8, v3, s[2:3]
	v_lshlrev_b32_e32 v10, 2, v3
	v_lshlrev_b32_e32 v4, 4, v1
	v_lshl_add_u64 v[10:11], s[14:15], 0, v[10:11]
	v_lshl_add_u64 v[56:57], v[10:11], 0, v[4:5]
	v_lshlrev_b32_e32 v66, 3, v0
	v_mov_b32_e32 v3, v5
	v_lshl_add_u64 v[64:65], v[2:3], 2, s[6:7]
	global_load_dwordx2 v[62:63], v66, s[4:5]
	global_load_dwordx4 v[14:17], v[56:57], off
	global_load_dwordx4 v[18:21], v[56:57], off offset:256
	global_load_dwordx4 v[22:25], v[56:57], off offset:512
	global_load_dwordx4 v[26:29], v[56:57], off offset:768
	global_load_dwordx4 v[30:33], v[56:57], off offset:1024
	global_load_dwordx4 v[34:37], v[56:57], off offset:1280
	global_load_dwordx4 v[38:41], v[56:57], off offset:1536
	global_load_dwordx4 v[42:45], v[56:57], off offset:1792
	global_load_dwordx3 v[2:4], v[54:55], off
	global_load_dword v10, v[64:65], off
	v_lshlrev_b32_e32 v67, 4, v1
	v_cmp_lt_u32_e64 s[4:5], -15, v7
	v_mov_b32_e32 v7, v5
	v_cmp_eq_u32_e64 s[6:7], 0, v1
	s_and_b64 s[6:7], s[2:3], s[6:7]
	s_waitcnt vmcnt(10)
	ds_write_b64 v66, v[62:63] offset:2048
	s_waitcnt lgkmcnt(0)
	s_barrier
	ds_read_b128 v[46:49], v67 offset:2048
	ds_read_b128 v[50:53], v67 offset:2304
	ds_read_b128 v[54:57], v67 offset:2560
	ds_read_b128 v[58:61], v67 offset:2816
	s_waitcnt vmcnt(9) lgkmcnt(3)
	v_mul_f32_e32 v15, v47, v15
	v_fmac_f32_e32 v15, v46, v14
	v_fmac_f32_e32 v15, v48, v16
	v_fmac_f32_e32 v15, v49, v17
	s_waitcnt vmcnt(8) lgkmcnt(2)
	v_mul_f32_e32 v19, v51, v19
	v_fmac_f32_e32 v19, v50, v18
	v_fmac_f32_e32 v19, v52, v20
	v_fmac_f32_e32 v19, v53, v21
	s_waitcnt vmcnt(7) lgkmcnt(1)
	v_mul_f32_e32 v23, v55, v23
	v_fmac_f32_e32 v23, v54, v22
	v_fmac_f32_e32 v23, v56, v24
	v_fmac_f32_e32 v23, v57, v25
	s_waitcnt vmcnt(6) lgkmcnt(0)
	v_mul_f32_e32 v27, v59, v27
	v_fmac_f32_e32 v27, v58, v26
	v_fmac_f32_e32 v27, v60, v28
	v_fmac_f32_e32 v27, v61, v29
	ds_read_b128 v[46:49], v67 offset:3072
	ds_read_b128 v[50:53], v67 offset:3328
	ds_read_b128 v[54:57], v67 offset:3584
	ds_read_b128 v[58:61], v67 offset:3840
	s_waitcnt vmcnt(5) lgkmcnt(3)
	v_mul_f32_e32 v31, v47, v31
	v_fmac_f32_e32 v31, v46, v30
	v_fmac_f32_e32 v31, v48, v32
	v_fmac_f32_e32 v31, v49, v33
	s_waitcnt vmcnt(4) lgkmcnt(2)
	v_mul_f32_e32 v35, v51, v35
	v_fmac_f32_e32 v35, v50, v34
	v_fmac_f32_e32 v35, v52, v36
	v_fmac_f32_e32 v35, v53, v37
	s_waitcnt vmcnt(3) lgkmcnt(1)
	v_mul_f32_e32 v39, v55, v39
	v_fmac_f32_e32 v39, v54, v38
	v_fmac_f32_e32 v39, v56, v40
	v_fmac_f32_e32 v39, v57, v41
	s_waitcnt vmcnt(2) lgkmcnt(0)
	v_mul_f32_e32 v43, v59, v43
	v_fmac_f32_e32 v43, v58, v42
	v_fmac_f32_e32 v43, v60, v44
	v_fmac_f32_e32 v43, v61, v45
	v_add_f32_e32 v8, 0, v15
	v_add_f32_e32 v8, v8, v19
	v_add_f32_e32 v8, v8, v23
	v_add_f32_e32 v8, v8, v27
	v_add_f32_e32 v8, v8, v31
	v_add_f32_e32 v8, v8, v35
	v_add_f32_e32 v8, v8, v39
	v_add_f32_e32 v8, v8, v43
	v_mov_b32_e32 v32, v5
	s_nop 1
	v_mov_b32_dpp v7, v8 row_mirror row_mask:0xf bank_mask:0xf
	s_nop 1
	v_add_f32_dpp v7, v7, v8 row_half_mirror row_mask:0xf bank_mask:0xf bound_ctrl:1
	s_nop 1
	v_mov_b32_dpp v32, v7 row_half_mirror row_mask:0xf bank_mask:0xf
	s_nop 1
	v_add_f32_dpp v7, v32, v7 quad_perm:[3,2,1,0] row_mask:0xf bank_mask:0xf bound_ctrl:1
	s_nop 1
	v_add_f32_dpp v7, v7, v7 quad_perm:[2,3,0,1] row_mask:0xf bank_mask:0xf bound_ctrl:1
	s_nop 1
	v_mov_b32_dpp v5, v7 quad_perm:[1,0,3,2] row_mask:0xf bank_mask:0xf
	s_and_saveexec_b64 s[2:3], s[6:7]
	v_add_f32_e32 v5, v7, v5
	v_lshlrev_b32_e32 v6, 2, v6
	ds_write_b32 v6, v5 offset:1856
	s_or_b64 exec, exec, s[2:3]
	s_waitcnt lgkmcnt(0)
	s_barrier
	s_and_saveexec_b64 s[2:3], vcc
	s_cbranch_execz .LBB0_27
	s_waitcnt vmcnt(1)
	v_mul_f32_e32 v3, 0.5, v3
	v_mul_f32_e32 v3, 0.15915494, v3
	v_cos_f32_e32 v8, v3
	v_sin_f32_e32 v6, v3
	v_add_f32_e32 v3, v2, v4
	v_mul_f32_e32 v3, 0.5, v3
	v_sub_f32_e32 v2, v2, v4
	v_mul_f32_e32 v2, 0.5, v2
	v_mul_f32_e32 v3, 0.15915494, v3
	v_mul_f32_e32 v2, 0.15915494, v2
	v_sin_f32_e32 v11, v3
	v_cos_f32_e32 v12, v2
	v_cos_f32_e32 v4, v3
	v_sin_f32_e32 v13, v2
	v_xor_b32_e32 v5, 0x80000000, v11
	v_mul_f32_e32 v2, v6, v12
	v_pk_mul_f32 v[4:5], v[8:9], v[4:5] op_sel_hi:[0,1]
	v_pk_mul_f32 v[6:7], v[6:7], v[12:13] op_sel_hi:[0,1] neg_lo:[0,1] neg_hi:[0,1]
	v_mul_f32_e32 v8, v8, v11
	s_and_saveexec_b64 s[6:7], s[4:5]
	s_xor_b64 s[4:5], exec, s[6:7]
	s_cbranch_execz .LBB0_25
	v_lshlrev_b32_e32 v9, 5, v9
	ds_write_b128 v9, v[4:7] offset:1024
	v_mov_b32_e32 v3, v7
	v_mov_b32_e32 v5, v8
	ds_write_b128 v9, v[2:5] offset:1040

	.amdhsa_kernel _Z11prep_kernelPKfS0_S0_S0_PDF16_P15HIP_vector_typeIfLj2EE
		.amdhsa_group_segment_fixed_size 4096
		.amdhsa_private_segment_fixed_size 0
		.amdhsa_kernarg_size 48
		.amdhsa_user_sgpr_count 2
		.amdhsa_user_sgpr_dispatch_ptr 0
		.amdhsa_user_sgpr_queue_ptr 0
		.amdhsa_user_sgpr_kernarg_segment_ptr 1
		.amdhsa_user_sgpr_dispatch_id 0
		.amdhsa_user_sgpr_kernarg_preload_length 0
		.amdhsa_user_sgpr_kernarg_preload_offset 0
		.amdhsa_user_sgpr_private_segment_size 0
		.amdhsa_uses_dynamic_stack 0
		.amdhsa_enable_private_segment 0
		.amdhsa_system_sgpr_workgroup_id_x 1
		.amdhsa_system_sgpr_workgroup_id_y 0
		.amdhsa_system_sgpr_workgroup_id_z 0
		.amdhsa_system_sgpr_workgroup_info 0
		.amdhsa_system_vgpr_workitem_id 0
		.amdhsa_next_free_vgpr 68
		.amdhsa_next_free_sgpr 16
		.amdhsa_accum_offset 68
		.amdhsa_reserve_vcc 1
		.amdhsa_float_round_mode_32 0
		.amdhsa_float_round_mode_16_64 0
		.amdhsa_float_denorm_mode_32 3
		.amdhsa_float_denorm_mode_16_64 3
		.amdhsa_dx10_clamp 1
		.amdhsa_ieee_mode 1
		.amdhsa_fp16_overflow 0
		.amdhsa_tg_split 0
		.amdhsa_exception_fp_ieee_invalid_op 0
		.amdhsa_exception_fp_denorm_src 0
		.amdhsa_exception_fp_ieee_div_zero 0
		.amdhsa_exception_fp_ieee_overflow 0
		.amdhsa_exception_fp_ieee_underflow 0
		.amdhsa_exception_fp_ieee_inexact 0
		.amdhsa_exception_int_div_zero 0
	.end_amdhsa_kernel

_Z9qsim_mainPKDF16_PK15HIP_vector_typeIfLj2EEPf:
	s_cmpk_gt_i32 s2, 0x3ff
	s_cbranch_scc1 .LBB1_11
	s_load_dwordx4 s[8:11], s[0:1], 0x0
	s_load_dwordx2 s[4:5], s[0:1], 0x10
	s_mul_i32 s1, s2, 56
	s_mul_hi_i32 s0, s2, 56
	v_mbcnt_lo_u32_b32 v2, -1, 0
	s_waitcnt lgkmcnt(0)
	s_add_u32 s6, s8, 0x20000
	s_addc_u32 s7, s9, 0
	s_add_u32 s20, s8, 0x80000
	s_addc_u32 s21, s9, 0
	s_add_u32 s12, s8, 0x38000
	s_addc_u32 s13, s9, 0
	s_add_i32 s22, s2, 0xfffffe00
	s_add_u32 s14, s4, s1
	s_addc_u32 s15, s5, s0
	s_mul_hi_i32 s0, s2, 0xa00
	s_mulk_i32 s2, 0xa00
	v_mbcnt_hi_u32_b32 v161, -1, v2
	s_add_u32 s10, s10, s2
	v_and_b32_e32 v2, 64, v161
	s_addc_u32 s11, s11, s0
	v_mov_b32_e32 v155, 0
	s_movk_i32 s23, 0x1000
	s_mov_b64 s[16:17], 0x28000
	v_mov_b32_e32 v1, 0x10000
	s_movk_i32 s24, 0x100
	v_mov_b32_e32 v158, 0x60
	v_mov_b32_e32 v159, 0x280
	v_mov_b32_e32 v160, 0x1280
	s_mov_b64 s[18:19], 0x40000
	s_mov_b32 s25, 0x40000
	v_xor_b32_e32 v162, 32, v161
	v_add_u32_e32 v163, 64, v2
	v_xor_b32_e32 v164, 16, v161
	v_mov_b32_e32 v165, 0x10a00
	s_nop 0
	s_nop 0
	s_branch .LBB1_3

amdhsa.kernels:
  - .agpr_count:     0
    .args:
      - .actual_access:  read_only
        .address_space:  global
        .offset:         0
        .size:           8
        .value_kind:     global_buffer
      - .actual_access:  read_only
        .address_space:  global
        .offset:         8
        .size:           8
        .value_kind:     global_buffer
      - .actual_access:  read_only
        .address_space:  global
        .offset:         16
        .size:           8
        .value_kind:     global_buffer
      - .actual_access:  read_only
        .address_space:  global
        .offset:         24
        .size:           8
        .value_kind:     global_buffer
      - .actual_access:  write_only
        .address_space:  global
        .offset:         32
        .size:           8
        .value_kind:     global_buffer
      - .actual_access:  write_only
        .address_space:  global
        .offset:         40
        .size:           8
        .value_kind:     global_buffer
    .group_segment_fixed_size: 4096
    .kernarg_segment_align: 8
    .kernarg_segment_size: 48
    .language:       OpenCL C
    .language_version:
      - 2
      - 0
    .max_flat_workgroup_size: 256
    .name:           _Z11prep_kernelPKfS0_S0_S0_PDF16_P15HIP_vector_typeIfLj2EE
    .private_segment_fixed_size: 0
    .sgpr_count:     22
    .sgpr_spill_count: 0
    .symbol:         _Z11prep_kernelPKfS0_S0_S0_PDF16_P15HIP_vector_typeIfLj2EE.kd
    .uniform_work_group_size: 1
    .uses_dynamic_stack: false
    .vgpr_count:     68
    .vgpr_spill_count: 0
    .wavefront_size: 64
  - .agpr_count:     0
    .args:
      - .actual_access:  read_only
        .address_space:  global
        .offset:         0
        .size:           8
        .value_kind:     global_buffer
      - .actual_access:  read_only
        .address_space:  global
        .offset:         8
        .size:           8
        .value_kind:     global_buffer
      - .actual_access:  write_only
        .address_space:  global
        .offset:         16
        .size:           8
        .value_kind:     global_buffer
    .group_segment_fixed_size: 68352
    .kernarg_segment_align: 8
    .kernarg_segment_size: 24
    .language:       OpenCL C
    .language_version:
      - 2
      - 0
    .max_flat_workgroup_size: 256
    .name:           _Z9qsim_mainPKDF16_PK15HIP_vector_typeIfLj2EEPf
    .private_segment_fixed_size: 0
    .sgpr_count:     41
    .sgpr_spill_count: 0
    .symbol:         _Z9qsim_mainPKDF16_PK15HIP_vector_typeIfLj2EEPf.kd
    .uniform_work_group_size: 1
    .uses_dynamic_stack: false
    .vgpr_count:     256
    .vgpr_spill_count: 0
    .wavefront_size: 64
